# final output (P12) stored with the nt hint as well: written once, never re-read by the kernel
# baseline (speedup 1.0000x reference)
.LBB0_1053:
	v_add_u32_e32 v4, s19, v40
	v_cmp_gt_i32_e32 vcc, s18, v4
	v_add_u32_e32 v109, s4, v40
	v_cmp_lt_i32_e64 s[0:1], s5, v109
	v_cndmask_b32_e32 v4, v40, v4, vcc
	v_lshlrev_b32_e32 v4, 2, v4
	v_ashrrev_i32_e32 v5, 31, v4
	v_lshlrev_b64 v[8:9], 2, v[4:5]
	v_lshl_add_u64 v[4:5], s[8:9], 0, v[8:9]
	global_load_dwordx4 v[4:7], v[4:5], off
	v_lshl_add_u64 v[8:9], s[10:11], 0, v[8:9]
	global_load_dwordx4 v[8:11], v[8:9], off
	v_cmp_gt_i32_e32 vcc, s18, v109
	s_waitcnt vmcnt(1)
	v_and_or_b32 v4, v4, 63, v77
	v_and_or_b32 v5, v5, 63, v77
	v_and_or_b32 v6, v6, 63, v77
	v_and_or_b32 v7, v7, 63, v77
	v_lshlrev_b32_e32 v4, 2, v4
	v_lshlrev_b32_e32 v5, 2, v5
	v_lshlrev_b32_e32 v6, 2, v6
	v_lshlrev_b32_e32 v7, 2, v7
	ds_bpermute_b32 v113, v4, v76
	ds_bpermute_b32 v114, v5, v76
	ds_bpermute_b32 v115, v6, v76
	ds_bpermute_b32 v116, v7, v76
	v_cndmask_b32_e32 v4, v40, v109, vcc
	v_ashrrev_i32_e32 v71, 31, v70
	v_ashrrev_i32_e32 v69, 31, v68
	v_ashrrev_i32_e32 v67, 31, v66
	v_ashrrev_i32_e32 v65, 31, v64
	v_ashrrev_i32_e32 v5, 31, v4
	v_lshlrev_b64 v[50:51], 11, v[70:71]
	v_lshlrev_b64 v[54:55], 11, v[68:69]
	v_lshlrev_b64 v[58:59], 11, v[66:67]
	v_lshlrev_b64 v[62:63], 11, v[64:65]
	v_lshlrev_b64 v[6:7], 12, v[4:5]
	v_lshl_add_u64 v[52:53], v[14:15], 0, v[50:51]
	v_lshl_add_u64 v[60:61], v[14:15], 0, v[58:59]
	v_lshl_add_u64 v[64:65], v[14:15], 0, v[62:63]
	v_lshl_add_u64 v[66:67], s[12:13], 0, v[54:55]
	v_lshl_add_u64 v[62:63], s[12:13], 0, v[62:63]
	v_lshl_add_u64 v[56:57], v[14:15], 0, v[54:55]
	v_lshl_add_u64 v[6:7], v[28:29], 0, v[6:7]
	global_load_dword v119, v[52:53], off
	global_load_dword v118, v[56:57], off
	global_load_dword v117, v[60:61], off
	global_load_dword v112, v[64:65], off
	global_load_dwordx2 v[40:41], v[6:7], off
	v_lshl_add_u64 v[60:61], s[12:13], 0, v[50:51]
	v_lshl_add_u64 v[50:51], v[66:67], 0, v[16:17]
	v_lshl_add_u64 v[58:59], s[12:13], 0, v[58:59]
	v_lshl_add_u64 v[132:133], v[62:63], 0, v[18:19]
	v_lshl_add_u64 v[52:53], v[58:59], 0, v[16:17]
	v_lshl_add_u64 v[54:55], v[62:63], 0, v[16:17]
	v_lshl_add_u64 v[56:57], v[60:61], 0, v[18:19]
	v_lshl_add_u64 v[68:69], v[66:67], 0, v[18:19]
	v_lshl_add_u64 v[70:71], v[58:59], 0, v[18:19]
	v_lshl_add_u64 v[134:135], v[60:61], 0, v[20:21]
	global_load_dword v127, v[50:51], off
	global_load_dword v123, v[52:53], off
	global_load_dword v120, v[54:55], off
	global_load_dword v130, v[56:57], off
	global_load_dword v128, v[68:69], off
	global_load_dword v126, v[70:71], off
	global_load_dword v122, v[132:133], off
	s_nop 0
	global_load_dword v133, v[134:135], off
	v_lshl_add_u64 v[68:69], v[66:67], 0, v[20:21]
	v_lshl_add_u64 v[134:135], v[62:63], 0, v[20:21]
	v_lshl_add_u64 v[142:143], v[66:67], 0, v[22:23]
	v_lshl_add_u64 v[144:145], v[58:59], 0, v[22:23]
	v_lshl_add_u64 v[146:147], v[62:63], 0, v[22:23]
	v_lshl_add_u64 v[148:149], v[60:61], 0, v[24:25]
	v_lshl_add_u64 v[70:71], v[58:59], 0, v[20:21]
	v_lshl_add_u64 v[138:139], v[60:61], 0, v[22:23]
	global_load_dwordx2 v[50:51], v[6:7], off offset:512
	global_load_dwordx2 v[52:53], v[6:7], off offset:1024
	global_load_dwordx2 v[54:55], v[6:7], off offset:1536
	global_load_dwordx2 v[56:57], v[6:7], off offset:2048
	global_load_dword v136, v[68:69], off
	global_load_dword v132, v[70:71], off
	global_load_dword v129, v[134:135], off
	global_load_dword v140, v[138:139], off
	s_nop 0
	global_load_dword v135, v[142:143], off
	global_load_dword v134, v[144:145], off
	global_load_dword v131, v[146:147], off
	s_nop 0
	global_load_dword v142, v[148:149], off
	v_lshl_add_u64 v[68:69], v[66:67], 0, v[24:25]
	v_lshl_add_u64 v[144:145], v[62:63], 0, v[24:25]
	v_lshl_add_u64 v[146:147], v[60:61], 0, v[26:27]
	v_lshl_add_u64 v[148:149], v[66:67], 0, v[26:27]
	v_lshl_add_u64 v[64:65], v[60:61], 0, v[16:17]
	v_lshl_add_u64 v[70:71], v[58:59], 0, v[24:25]
	v_lshl_add_u64 v[152:153], v[58:59], 0, v[26:27]
	v_lshl_add_u64 v[154:155], v[62:63], 0, v[26:27]
	v_lshl_add_u64 v[60:61], v[60:61], 0, v[12:13]
	global_load_dword v143, v[68:69], off
	global_load_dword v139, v[70:71], off
	global_load_dword v137, v[144:145], off
	s_nop 0
	global_load_dword v147, v[146:147], off
	s_nop 0
	global_load_dword v144, v[148:149], off
	global_load_dword v141, v[152:153], off
	global_load_dword v138, v[154:155], off
	s_nop 0
	global_load_dword v148, v[60:61], off
	v_lshlrev_b32_e32 v4, 2, v4
	v_ashrrev_i32_e32 v5, 31, v4
	v_lshl_add_u64 v[66:67], v[66:67], 0, v[12:13]
	v_lshl_add_u64 v[4:5], v[4:5], 2, s[14:15]
	v_lshl_add_u64 v[68:69], v[58:59], 0, v[12:13]
	v_lshl_add_u64 v[70:71], v[62:63], 0, v[12:13]
	global_load_dword v151, v[64:65], off
	global_load_dwordx2 v[58:59], v[6:7], off offset:2560
	global_load_dwordx2 v[60:61], v[6:7], off offset:3072
	global_load_dwordx2 v[62:63], v[6:7], off offset:3584
	global_load_dword v149, v[66:67], off
	global_load_dword v146, v[68:69], off
	global_load_dword v145, v[70:71], off
	s_nop 0
	global_load_dwordx4 v[4:7], v[4:5], off
	v_cvt_pk_f32_fp8_e32 v[64:65], v75
	v_cvt_pk_f32_fp8_sdwa v[66:67], v75 src0_sel:WORD_1
	v_cvt_pk_f32_fp8_e32 v[68:69], v74
	v_cvt_pk_f32_fp8_sdwa v[70:71], v74 src0_sel:WORD_1
	v_pk_fma_f32 v[64:65], v[0:1], v[64:65], 0 op_sel_hi:[0,1,0]
	v_pk_fma_f32 v[66:67], v[0:1], v[66:67], 0 op_sel_hi:[0,1,0]
	v_pk_fma_f32 v[64:65], v[0:1], v[68:69], v[64:65] op_sel:[1,0,0]
	v_pk_fma_f32 v[66:67], v[0:1], v[70:71], v[66:67] op_sel:[1,0,0]
	v_cvt_pk_f32_fp8_e32 v[68:69], v111
	v_cvt_pk_f32_fp8_sdwa v[70:71], v111 src0_sel:WORD_1
	v_lshlrev_b32_e32 v74, 16, v46
	v_and_b32_e32 v75, 0xffff0000, v46
	v_pk_fma_f32 v[64:65], v[2:3], v[68:69], v[64:65] op_sel_hi:[0,1,1]
	v_pk_fma_f32 v[66:67], v[2:3], v[70:71], v[66:67] op_sel_hi:[0,1,1]
	v_cvt_pk_f32_fp8_e32 v[68:69], v110
	v_cvt_pk_f32_fp8_sdwa v[70:71], v110 src0_sel:WORD_1
	v_add_u32_e32 v110, 0, v78
	v_lshlrev_b32_e32 v46, 16, v47
	v_pk_fma_f32 v[68:69], v[2:3], v[68:69], v[64:65] op_sel:[1,0,0]
	v_pk_fma_f32 v[70:71], v[2:3], v[70:71], v[66:67] op_sel:[1,0,0]
	ds_read_b128 v[64:67], v110
	v_and_b32_e32 v47, 0xffff0000, v47
	v_cvt_pk_f32_fp8_sdwa v[152:153], v105 src0_sel:WORD_1
	v_cvt_pk_f32_fp8_sdwa v[154:155], v102 src0_sel:WORD_1
	s_or_b64 s[16:17], s[0:1], s[16:17]
	s_waitcnt lgkmcnt(0)
	v_pk_fma_f32 v[46:47], v[66:67], v[70:71], v[46:47]
	v_pk_fma_f32 v[64:65], v[64:65], v[68:69], v[74:75]
	v_cvt_pk_f32_fp8_e32 v[66:67], v150
	v_cvt_pk_f32_fp8_sdwa v[68:69], v150 src0_sel:WORD_1
	v_cvt_pk_f32_fp8_e32 v[70:71], v121
	v_cvt_pk_f32_fp8_sdwa v[74:75], v121 src0_sel:WORD_1
	v_pk_fma_f32 v[66:67], v[0:1], v[66:67], 0 op_sel_hi:[0,1,0]
	v_pk_fma_f32 v[68:69], v[0:1], v[68:69], 0 op_sel_hi:[0,1,0]
	v_pk_fma_f32 v[66:67], v[0:1], v[70:71], v[66:67] op_sel:[1,0,0]
	v_pk_fma_f32 v[68:69], v[0:1], v[74:75], v[68:69] op_sel:[1,0,0]
	v_cvt_pk_f32_fp8_e32 v[70:71], v125
	v_cvt_pk_f32_fp8_sdwa v[74:75], v125 src0_sel:WORD_1
	v_and_b32_e32 v125, 0xffff0000, v48
	s_waitcnt vmcnt(7)
	v_mov_b32_e32 v150, v151
	v_pk_fma_f32 v[66:67], v[2:3], v[70:71], v[66:67] op_sel_hi:[0,1,1]
	v_pk_fma_f32 v[68:69], v[2:3], v[74:75], v[68:69] op_sel_hi:[0,1,1]
	v_cvt_pk_f32_fp8_e32 v[70:71], v124
	v_cvt_pk_f32_fp8_sdwa v[74:75], v124 src0_sel:WORD_1
	v_lshlrev_b32_e32 v124, 16, v48
	v_lshlrev_b32_e32 v48, 16, v49
	v_pk_fma_f32 v[70:71], v[2:3], v[70:71], v[66:67] op_sel:[1,0,0]
	v_pk_fma_f32 v[74:75], v[2:3], v[74:75], v[68:69] op_sel:[1,0,0]
	ds_read_b128 v[66:69], v110 offset:1024
	v_and_b32_e32 v49, 0xffff0000, v49
	v_mov_b32_e32 v121, v127
	v_mov_b32_e32 v111, v117
	s_waitcnt lgkmcnt(0)
	v_pk_fma_f32 v[66:67], v[66:67], v[70:71], v[124:125]
	v_pk_fma_f32 v[48:49], v[68:69], v[74:75], v[48:49]
	v_mov_b32_e32 v70, v65
	v_mov_b32_e32 v71, v67
	v_mov_b32_e32 v68, v64
	v_mov_b32_e32 v69, v66
	v_pk_mul_f32 v[70:71], v[70:71], v[70:71]
	v_mov_b32_e32 v74, v47
	v_mov_b32_e32 v75, v49
	v_pk_fma_f32 v[68:69], v[68:69], v[68:69], v[70:71]
	v_mov_b32_e32 v70, v46
	v_mov_b32_e32 v71, v48
	v_pk_mul_f32 v[74:75], v[74:75], v[74:75]
	v_cvt_pk_f32_fp8_e32 v[124:125], v105
	v_pk_fma_f32 v[70:71], v[70:71], v[70:71], v[74:75]
	s_nop 0
	v_pk_add_f32 v[74:75], v[68:69], v[70:71]
	v_cvt_pk_f32_fp8_e32 v[68:69], v106
	v_cvt_pk_f32_fp8_sdwa v[70:71], v106 src0_sel:WORD_1
	v_pk_add_f32 v[74:75], v[74:75], v[74:75] op_sel:[0,1] op_sel_hi:[1,0]
	v_pk_fma_f32 v[68:69], v[0:1], v[68:69], 0 op_sel_hi:[0,1,0]
	v_pk_fma_f32 v[68:69], v[0:1], v[124:125], v[68:69] op_sel:[1,0,0]
	v_cvt_pk_f32_fp8_e32 v[124:125], v108
	v_pk_fma_f32 v[70:71], v[0:1], v[70:71], 0 op_sel_hi:[0,1,0]
	v_pk_fma_f32 v[70:71], v[0:1], v[152:153], v[70:71] op_sel:[1,0,0]
	v_cvt_pk_f32_fp8_sdwa v[152:153], v108 src0_sel:WORD_1
	v_pk_fma_f32 v[68:69], v[2:3], v[124:125], v[68:69] op_sel_hi:[0,1,1]
	v_cvt_pk_f32_fp8_e32 v[124:125], v107
	v_cvt_pk_f32_fp8_sdwa v[106:107], v107 src0_sel:WORD_1
	v_pk_fma_f32 v[70:71], v[2:3], v[152:153], v[70:71] op_sel_hi:[0,1,1]
	v_lshlrev_b32_e32 v152, 16, v44
	v_pk_fma_f32 v[124:125], v[2:3], v[124:125], v[68:69] op_sel:[1,0,0]
	v_pk_fma_f32 v[106:107], v[2:3], v[106:107], v[70:71] op_sel:[1,0,0]
	ds_read_b128 v[68:71], v110 offset:2048
	v_and_b32_e32 v153, 0xffff0000, v44
	v_lshlrev_b32_e32 v44, 16, v45
	v_and_b32_e32 v45, 0xffff0000, v45
	v_mov_b32_e32 v108, v126
	s_waitcnt lgkmcnt(0)
	v_pk_fma_f32 v[44:45], v[70:71], v[106:107], v[44:45]
	v_pk_fma_f32 v[68:69], v[68:69], v[124:125], v[152:153]
	v_pk_mul_f32 v[70:71], v[44:45], v[44:45]
	v_pk_mul_f32 v[106:107], v[68:69], v[68:69]
	v_cvt_pk_f32_fp8_e32 v[152:153], v102
	v_pk_mov_b32 v[124:125], v[106:107], v[70:71] op_sel:[1,0]
	v_mov_b32_e32 v107, v71
	v_cvt_pk_f32_fp8_e32 v[70:71], v101
	v_pk_add_f32 v[106:107], v[124:125], v[106:107]
	v_cvt_pk_f32_fp8_sdwa v[124:125], v101 src0_sel:WORD_1
	v_pk_fma_f32 v[70:71], v[0:1], v[70:71], 0 op_sel_hi:[0,1,0]
	v_pk_fma_f32 v[70:71], v[0:1], v[152:153], v[70:71] op_sel:[1,0,0]
	v_cvt_pk_f32_fp8_e32 v[152:153], v104
	v_cvt_pk_f32_fp8_sdwa v[104:105], v104 src0_sel:WORD_1
	v_pk_fma_f32 v[124:125], v[0:1], v[124:125], 0 op_sel_hi:[0,1,0]
	v_pk_fma_f32 v[124:125], v[0:1], v[154:155], v[124:125] op_sel:[1,0,0]
	v_pk_fma_f32 v[70:71], v[2:3], v[152:153], v[70:71] op_sel_hi:[0,1,1]
	v_pk_fma_f32 v[104:105], v[2:3], v[104:105], v[124:125] op_sel_hi:[0,1,1]
	v_cvt_pk_f32_fp8_e32 v[124:125], v103
	v_cvt_pk_f32_fp8_sdwa v[102:103], v103 src0_sel:WORD_1
	v_lshlrev_b32_e32 v152, 16, v42
	v_and_b32_e32 v153, 0xffff0000, v42
	v_pk_fma_f32 v[70:71], v[2:3], v[124:125], v[70:71] op_sel:[1,0,0]
	v_pk_fma_f32 v[124:125], v[2:3], v[102:103], v[104:105] op_sel:[1,0,0]
	ds_read_b128 v[102:105], v110 offset:3072
	v_lshlrev_b32_e32 v42, 16, v43
	v_and_b32_e32 v43, 0xffff0000, v43
	s_waitcnt lgkmcnt(0)
	v_pk_fma_f32 v[42:43], v[104:105], v[124:125], v[42:43]
	v_cvt_pk_f32_fp8_sdwa v[104:105], v72 src0_sel:WORD_1
	v_cvt_pk_f32_fp8_e32 v[124:125], v100
	v_cvt_pk_f32_fp8_sdwa v[100:101], v100 src0_sel:WORD_1
	v_pk_fma_f32 v[70:71], v[102:103], v[70:71], v[152:153]
	v_cvt_pk_f32_fp8_e32 v[102:103], v72
	v_pk_fma_f32 v[104:105], v[0:1], v[104:105], 0 op_sel_hi:[0,1,0]
	v_pk_fma_f32 v[100:101], v[0:1], v[100:101], v[104:105] op_sel:[1,0,0]
	v_cvt_pk_f32_fp8_e32 v[104:105], v99
	v_pk_fma_f32 v[102:103], v[0:1], v[102:103], 0 op_sel_hi:[0,1,0]
	v_pk_fma_f32 v[102:103], v[0:1], v[124:125], v[102:103] op_sel:[1,0,0]
	v_cvt_pk_f32_fp8_sdwa v[124:125], v99 src0_sel:WORD_1
	v_pk_fma_f32 v[102:103], v[2:3], v[104:105], v[102:103] op_sel_hi:[0,1,1]
	v_cvt_pk_f32_fp8_e32 v[104:105], v73
	v_cvt_pk_f32_fp8_sdwa v[72:73], v73 src0_sel:WORD_1
	v_pk_fma_f32 v[100:101], v[2:3], v[124:125], v[100:101] op_sel_hi:[0,1,1]
	v_lshlrev_b32_e32 v124, 16, v38
	v_pk_fma_f32 v[104:105], v[2:3], v[104:105], v[102:103] op_sel:[1,0,0]
	v_pk_fma_f32 v[72:73], v[2:3], v[72:73], v[100:101] op_sel:[1,0,0]
	ds_read_b128 v[100:103], v110 offset:4096
	v_and_b32_e32 v125, 0xffff0000, v38
	v_lshlrev_b32_e32 v38, 16, v39
	v_and_b32_e32 v39, 0xffff0000, v39
	s_waitcnt lgkmcnt(0)
	v_pk_fma_f32 v[38:39], v[102:103], v[72:73], v[38:39]
	v_pk_fma_f32 v[72:73], v[100:101], v[104:105], v[124:125]
	v_pk_add_f32 v[100:101], v[106:107], v[106:107] op_sel:[0,1] op_sel_hi:[1,0]
	v_mul_f32_e32 v99, v72, v72
	v_mul_f32_e32 v102, v73, v73
	v_mov_b32_e32 v75, v99
	v_mov_b32_e32 v101, v102
	v_pk_add_f32 v[74:75], v[74:75], v[100:101]
	v_mul_f32_e32 v100, v71, v71
	v_mul_f32_e32 v103, v38, v38
	v_pk_fma_f32 v[100:101], v[70:71], v[70:71], v[100:101] op_sel_hi:[1,1,0]
	v_mul_f32_e32 v102, v43, v43
	v_mul_f32_e32 v104, v39, v39
	v_mov_b32_e32 v101, v103
	v_pk_fma_f32 v[102:103], v[42:43], v[42:43], v[102:103] op_sel_hi:[1,1,0]
	v_mov_b32_e32 v106, v130
	v_mov_b32_e32 v103, v104
	v_pk_add_f32 v[100:101], v[100:101], v[102:103]
	v_cvt_pk_f32_fp8_sdwa v[102:103], v95 src0_sel:WORD_1
	v_cvt_pk_f32_fp8_e32 v[104:105], v98
	v_cvt_pk_f32_fp8_sdwa v[98:99], v98 src0_sel:WORD_1
	v_pk_add_f32 v[74:75], v[74:75], v[100:101]
	v_cvt_pk_f32_fp8_e32 v[100:101], v95
	v_pk_fma_f32 v[102:103], v[0:1], v[102:103], 0 op_sel_hi:[0,1,0]
	v_pk_fma_f32 v[98:99], v[0:1], v[98:99], v[102:103] op_sel:[1,0,0]
	v_cvt_pk_f32_fp8_e32 v[102:103], v97
	v_pk_fma_f32 v[100:101], v[0:1], v[100:101], 0 op_sel_hi:[0,1,0]
	v_pk_fma_f32 v[100:101], v[0:1], v[104:105], v[100:101] op_sel:[1,0,0]
	v_cvt_pk_f32_fp8_sdwa v[104:105], v97 src0_sel:WORD_1
	v_pk_fma_f32 v[100:101], v[2:3], v[102:103], v[100:101] op_sel_hi:[0,1,1]
	v_cvt_pk_f32_fp8_e32 v[102:103], v96
	v_cvt_pk_f32_fp8_sdwa v[96:97], v96 src0_sel:WORD_1
	v_pk_fma_f32 v[98:99], v[2:3], v[104:105], v[98:99] op_sel_hi:[0,1,1]
	v_lshlrev_b32_e32 v104, 16, v36
	v_pk_fma_f32 v[100:101], v[2:3], v[102:103], v[100:101] op_sel:[1,0,0]
	v_pk_fma_f32 v[102:103], v[2:3], v[96:97], v[98:99] op_sel:[1,0,0]
	ds_read_b128 v[96:99], v110 offset:5120
	v_and_b32_e32 v105, 0xffff0000, v36
	v_lshlrev_b32_e32 v36, 16, v37
	v_and_b32_e32 v37, 0xffff0000, v37
	v_mov_b32_e32 v125, v123
	s_waitcnt lgkmcnt(0)
	v_pk_fma_f32 v[36:37], v[98:99], v[102:103], v[36:37]
	v_pk_fma_f32 v[96:97], v[96:97], v[100:101], v[104:105]
	v_pk_mul_f32 v[98:99], v[36:37], v[36:37]
	v_pk_mul_f32 v[100:101], v[96:97], v[96:97]
	v_cvt_pk_f32_fp8_e32 v[104:105], v94
	v_pk_mov_b32 v[102:103], v[100:101], v[98:99] op_sel:[1,0]
	v_mov_b32_e32 v101, v99
	v_pk_add_f32 v[98:99], v[102:103], v[100:101]
	v_cvt_pk_f32_fp8_sdwa v[102:103], v91 src0_sel:WORD_1
	v_cvt_pk_f32_fp8_sdwa v[94:95], v94 src0_sel:WORD_1
	v_cvt_pk_f32_fp8_e32 v[100:101], v91
	v_mov_b32_e32 v124, v120
	v_pk_fma_f32 v[102:103], v[0:1], v[102:103], 0 op_sel_hi:[0,1,0]
	v_pk_fma_f32 v[94:95], v[0:1], v[94:95], v[102:103] op_sel:[1,0,0]
	v_cvt_pk_f32_fp8_e32 v[102:103], v93
	v_pk_fma_f32 v[100:101], v[0:1], v[100:101], 0 op_sel_hi:[0,1,0]
	v_pk_fma_f32 v[100:101], v[0:1], v[104:105], v[100:101] op_sel:[1,0,0]
	v_cvt_pk_f32_fp8_sdwa v[104:105], v93 src0_sel:WORD_1
	v_pk_fma_f32 v[100:101], v[2:3], v[102:103], v[100:101] op_sel_hi:[0,1,1]
	v_cvt_pk_f32_fp8_e32 v[102:103], v92
	v_cvt_pk_f32_fp8_sdwa v[92:93], v92 src0_sel:WORD_1
	v_pk_fma_f32 v[94:95], v[2:3], v[104:105], v[94:95] op_sel_hi:[0,1,1]
	v_lshlrev_b32_e32 v104, 16, v34
	v_pk_fma_f32 v[100:101], v[2:3], v[102:103], v[100:101] op_sel:[1,0,0]
	v_pk_fma_f32 v[102:103], v[2:3], v[92:93], v[94:95] op_sel:[1,0,0]
	ds_read_b128 v[92:95], v110 offset:6144
	v_and_b32_e32 v105, 0xffff0000, v34
	v_lshlrev_b32_e32 v34, 16, v35
	v_and_b32_e32 v35, 0xffff0000, v35
	v_mov_b32_e32 v107, v122
	s_waitcnt lgkmcnt(0)
	v_pk_fma_f32 v[34:35], v[94:95], v[102:103], v[34:35]
	v_pk_fma_f32 v[92:93], v[92:93], v[100:101], v[104:105]
	v_cvt_pk_f32_fp8_e32 v[94:95], v87
	v_cvt_pk_f32_fp8_sdwa v[100:101], v87 src0_sel:WORD_1
	v_cvt_pk_f32_fp8_e32 v[102:103], v90
	v_cvt_pk_f32_fp8_sdwa v[90:91], v90 src0_sel:WORD_1
	v_pk_fma_f32 v[94:95], v[0:1], v[94:95], 0 op_sel_hi:[0,1,0]
	v_pk_fma_f32 v[100:101], v[0:1], v[100:101], 0 op_sel_hi:[0,1,0]
	v_pk_fma_f32 v[94:95], v[0:1], v[102:103], v[94:95] op_sel:[1,0,0]
	v_pk_fma_f32 v[0:1], v[0:1], v[90:91], v[100:101] op_sel:[1,0,0]
	v_cvt_pk_f32_fp8_e32 v[90:91], v89
	v_cvt_pk_f32_fp8_sdwa v[100:101], v89 src0_sel:WORD_1
	v_mov_b32_e32 v105, v128
	v_mov_b32_e32 v102, v136
	v_pk_fma_f32 v[90:91], v[2:3], v[90:91], v[94:95] op_sel_hi:[0,1,1]
	v_cvt_pk_f32_fp8_e32 v[94:95], v88
	v_cvt_pk_f32_fp8_sdwa v[88:89], v88 src0_sel:WORD_1
	v_pk_fma_f32 v[0:1], v[2:3], v[100:101], v[0:1] op_sel_hi:[0,1,1]
	v_mov_b32_e32 v101, v133
	v_pk_fma_f32 v[90:91], v[2:3], v[94:95], v[90:91] op_sel:[1,0,0]
	v_pk_fma_f32 v[88:89], v[2:3], v[88:89], v[0:1] op_sel:[1,0,0]
	ds_read_b128 v[0:3], v110 offset:7168
	v_lshlrev_b32_e32 v94, 16, v32
	v_and_b32_e32 v95, 0xffff0000, v32
	v_lshlrev_b32_e32 v32, 16, v33
	v_and_b32_e32 v33, 0xffff0000, v33
	s_waitcnt lgkmcnt(0)
	v_pk_fma_f32 v[32:33], v[2:3], v[88:89], v[32:33]
	v_pk_fma_f32 v[88:89], v[0:1], v[90:91], v[94:95]
	v_pk_add_f32 v[0:1], v[74:75], v[74:75] op_sel:[0,1] op_sel_hi:[1,0]
	v_mul_f32_e32 v2, v88, v88
	v_mul_f32_e32 v87, v89, v89
	v_mov_b32_e32 v1, v2
	v_pk_add_f32 v[2:3], v[98:99], v[98:99] op_sel:[0,1] op_sel_hi:[1,0]
	v_mul_f32_e32 v74, v35, v35
	v_mov_b32_e32 v3, v87
	v_pk_add_f32 v[0:1], v[0:1], v[2:3]
	v_mul_f32_e32 v2, v93, v93
	v_mul_f32_e32 v90, v32, v32
	v_mul_f32_e32 v91, v33, v33
	v_pk_fma_f32 v[2:3], v[92:93], v[92:93], v[2:3] op_sel_hi:[1,1,0]
	v_pk_fma_f32 v[74:75], v[34:35], v[34:35], v[74:75] op_sel_hi:[1,1,0]
	v_mov_b32_e32 v3, v90
	v_mov_b32_e32 v75, v91
	v_pk_add_f32 v[2:3], v[2:3], v[74:75]
	v_mov_b32_e32 v95, v142
	v_pk_add_f32 v[0:1], v[0:1], v[2:3]
	v_mov_b32_e32 v91, v147
	v_add_f32_e32 v0, v0, v1
	ds_bpermute_b32 v1, v79, v0
	v_mov_b32_e32 v87, v148
	v_mov_b32_e32 v100, v135
	v_mov_b32_e32 v98, v143
	v_mov_b32_e32 v94, v144
	s_waitcnt lgkmcnt(0)
	v_add_f32_e32 v0, v0, v1
	ds_bpermute_b32 v1, v80, v0
	s_waitcnt vmcnt(3)
	v_mov_b32_e32 v90, v149
	v_mov_b32_e32 v104, v132
	v_mov_b32_e32 v99, v134
	v_mov_b32_e32 v103, v129
	s_waitcnt lgkmcnt(0)
	v_add_f32_e32 v0, v0, v1
	ds_bpermute_b32 v1, v81, v0
	s_waitcnt lgkmcnt(0)
	v_add_f32_e32 v0, v0, v1
	ds_bpermute_b32 v1, v82, v0
	s_waitcnt lgkmcnt(0)
	v_add_f32_e32 v0, v0, v1
	ds_bpermute_b32 v1, v83, v0
	s_waitcnt lgkmcnt(0)
	v_add_f32_e32 v0, v0, v1
	ds_bpermute_b32 v1, v84, v0
	s_waitcnt lgkmcnt(0)
	v_add_f32_e32 v0, v0, v1
	v_fmamk_f32 v0, v0, 0x3a000000, v85
	v_cmp_gt_f32_e32 vcc, s20, v0
	v_mul_f32_e32 v1, 0x4f800000, v0
	s_nop 0
	v_cndmask_b32_e32 v0, v0, v1, vcc
	v_sqrt_f32_e32 v1, v0
	s_nop 0
	v_add_u32_e32 v2, -1, v1
	v_fma_f32 v3, -v2, v1, v0
	v_cmp_ge_f32_e64 s[2:3], 0, v3
	v_add_u32_e32 v3, 1, v1
	s_nop 0
	v_cndmask_b32_e64 v2, v1, v2, s[2:3]
	v_fma_f32 v1, -v3, v1, v0
	v_cmp_lt_f32_e64 s[2:3], 0, v1
	s_nop 1
	v_cndmask_b32_e64 v1, v2, v3, s[2:3]
	v_mul_f32_e32 v2, 0x37800000, v1
	v_cndmask_b32_e32 v1, v1, v2, vcc
	v_cmp_class_f32_e32 vcc, v0, v86
	s_nop 1
	v_cndmask_b32_e32 v0, v1, v0, vcc
	v_div_scale_f32 v1, s[2:3], v0, v0, 1.0
	v_rcp_f32_e32 v2, v1
	s_nop 0
	v_fma_f32 v3, -v1, v2, 1.0
	v_fmac_f32_e32 v2, v3, v2
	v_div_scale_f32 v3, vcc, 1.0, v0, 1.0
	v_mul_f32_e32 v74, v3, v2
	v_fma_f32 v75, -v1, v74, v3
	v_fmac_f32_e32 v74, v75, v2
	v_fma_f32 v1, -v1, v74, v3
	v_div_fmas_f32 v1, v1, v2, v74
	v_div_fixup_f32 v74, v1, v0, 1.0
	ds_read_b128 v[0:3], v110 offset:8192
	v_pk_mul_f32 v[64:65], v[64:65], v[74:75] op_sel_hi:[1,0]
	v_pk_mul_f32 v[46:47], v[46:47], v[74:75] op_sel_hi:[1,0]
	v_pk_mul_f32 v[48:49], v[48:49], v[74:75] op_sel_hi:[1,0]
	v_pk_mul_f32 v[44:45], v[44:45], v[74:75] op_sel_hi:[1,0]
	s_waitcnt lgkmcnt(0)
	v_pk_mul_f32 v[2:3], v[2:3], v[46:47]
	v_pk_mul_f32 v[0:1], v[0:1], v[64:65]
	global_store_dwordx4 v[30:31], v[0:3], off offset:-4096 nt
	ds_read_b128 v[0:3], v110 offset:9216
	v_pk_mul_f32 v[46:47], v[66:67], v[74:75] op_sel_hi:[1,0]
	v_pk_mul_f32 v[42:43], v[42:43], v[74:75] op_sel_hi:[1,0]
	v_pk_mul_f32 v[38:39], v[38:39], v[74:75] op_sel_hi:[1,0]
	v_pk_mul_f32 v[36:37], v[36:37], v[74:75] op_sel_hi:[1,0]
	s_waitcnt lgkmcnt(0)
	v_pk_mul_f32 v[2:3], v[2:3], v[48:49]
	v_pk_mul_f32 v[0:1], v[0:1], v[46:47]
	global_store_dwordx4 v[30:31], v[0:3], off offset:-3072 nt
	ds_read_b128 v[0:3], v110 offset:10240
	v_pk_mul_f32 v[46:47], v[68:69], v[74:75] op_sel_hi:[1,0]
	v_pk_mul_f32 v[34:35], v[34:35], v[74:75] op_sel_hi:[1,0]
	v_pk_mul_f32 v[32:33], v[32:33], v[74:75] op_sel_hi:[1,0]
	v_add_u32_e32 v68, v9, v114
	s_waitcnt lgkmcnt(0)
	v_pk_mul_f32 v[2:3], v[2:3], v[44:45]
	v_pk_mul_f32 v[0:1], v[0:1], v[46:47]
	global_store_dwordx4 v[30:31], v[0:3], off offset:-2048 nt
	ds_read_b128 v[0:3], v110 offset:11264
	v_pk_mul_f32 v[44:45], v[70:71], v[74:75] op_sel_hi:[1,0]
	v_add_u32_e32 v70, v8, v113
	v_add_u32_e32 v66, v10, v115
	v_add_u32_e32 v64, v11, v116
	s_waitcnt lgkmcnt(0)
	v_pk_mul_f32 v[2:3], v[2:3], v[42:43]
	v_pk_mul_f32 v[0:1], v[0:1], v[44:45]
	global_store_dwordx4 v[30:31], v[0:3], off offset:-1024 nt
	ds_read_b128 v[0:3], v110 offset:12288
	v_pk_mul_f32 v[42:43], v[72:73], v[74:75] op_sel_hi:[1,0]
	v_mov_b32_e32 v72, v140
	v_mov_b64_e32 v[44:45], v[52:53]
	v_mov_b64_e32 v[48:49], v[50:51]
	s_waitcnt lgkmcnt(0)
	v_pk_mul_f32 v[2:3], v[2:3], v[38:39]
	v_pk_mul_f32 v[0:1], v[0:1], v[42:43]
	global_store_dwordx4 v[30:31], v[0:3], off nt
	ds_read_b128 v[0:3], v110 offset:13312
	v_pk_mul_f32 v[38:39], v[96:97], v[74:75] op_sel_hi:[1,0]
	v_mov_b64_e32 v[42:43], v[54:55]
	v_mov_b64_e32 v[46:47], v[40:41]
	v_mov_b32_e32 v97, v139
	s_waitcnt lgkmcnt(0)
	v_pk_mul_f32 v[0:1], v[0:1], v[38:39]
	v_pk_mul_f32 v[2:3], v[2:3], v[36:37]
	global_store_dwordx4 v[30:31], v[0:3], off offset:1024 nt
	ds_read_b128 v[0:3], v110 offset:14336
	v_pk_mul_f32 v[36:37], v[92:93], v[74:75] op_sel_hi:[1,0]
	v_mov_b64_e32 v[38:39], v[56:57]
	v_mov_b32_e32 v93, v141
	v_mov_b32_e32 v73, v131
	s_waitcnt lgkmcnt(0)
	v_pk_mul_f32 v[0:1], v[0:1], v[36:37]
	v_pk_mul_f32 v[2:3], v[2:3], v[34:35]
	global_store_dwordx4 v[30:31], v[0:3], off offset:2048 nt
	ds_read_b128 v[0:3], v110 offset:15360
	v_pk_mul_f32 v[34:35], v[88:89], v[74:75] op_sel_hi:[1,0]
	v_mov_b32_e32 v75, v119
	v_mov_b32_e32 v74, v118
	v_mov_b64_e32 v[36:37], v[58:59]
	s_waitcnt lgkmcnt(0)
	v_pk_mul_f32 v[0:1], v[0:1], v[34:35]
	v_pk_mul_f32 v[2:3], v[2:3], v[32:33]
	global_store_dwordx4 v[30:31], v[0:3], off offset:3072 nt
	v_lshl_add_u64 v[30:31], v[30:31], 0, s[6:7]
	v_mov_b64_e32 v[32:33], v[62:63]
	v_mov_b64_e32 v[34:35], v[60:61]
	s_waitcnt vmcnt(10)
	v_mov_b32_e32 v89, v146
	v_mov_b32_e32 v110, v112
	v_mov_b32_e32 v96, v137
	v_mov_b32_e32 v92, v138
	s_waitcnt vmcnt(9)
	v_mov_b32_e32 v88, v145
	v_mov_b32_e32 v40, v109
	s_waitcnt vmcnt(8)
	v_mov_b64_e32 v[2:3], v[6:7]
	v_mov_b64_e32 v[0:1], v[4:5]
	s_andn2_b64 exec, exec, s[16:17]
	s_cbranch_execnz .LBB0_1053
